# mLSTM chain: strips remapped so SIMD partner waves own strips (s, 7-s), balancing the triangular work across SIMDs
# baseline (speedup 1.0000x reference)
; #define LAS __attribute__((address_space(3)))
; __device__ __forceinline__ int opaque(int x) { asm volatile("" : "+v"(x)); return x; }
; __device__ __forceinline__ void p2_mlstm_chain(Frame& F, const Args& A, int ch) {
;     const int b = ch >> 2, h = ch & 3, tid = opaque(F.tid), lane = tid & 63, w = F.wave, tl = lane & 15, fq = lane >> 4;
;     const bf16* proj = (const bf16*)(F.ws + WS_PROJ); const float* gates = (const float*)(F.ws + WS_GATES); bf16* ycat = (bf16*)(F.ws + WS_R2);
;     const float* ghead = A.in[5] + h * 128;
;     LAS unsigned char* L = F.lds;
;     LAS float* sA = (LAS float*)(L + ML_A); LAS float* sM = (LAS float*)(L + ML_M); LAS float* sLF = (LAS float*)(L + ML_LF); LAS float* sMC = (LAS float*)(L + ML_MC);
;     LAS float* ns = (LAS float*)(L + ML_NS); LAS float* sWK = (LAS float*)(L + ML_WK);
;     __syncthreads();
;     {
; #pragma unroll
;       for (int cc = 0; cc < 2; ++cc) { const int c = 2 * w + cc, p0 = c * 128 + 2 * lane; const size_t gi = ((size_t)b * SEQ + p0) * 8;
;           const float i0 = gates[gi + h], f0 = gates[gi + 4 + h], i1 = gates[gi + 8 + h], f1 = gates[gi + 12 + h];
;           float sc = f0 + f1;
; #pragma unroll
;           for (int o = 1; o < 64; o <<= 1) { const float t = __shfl_up(sc, o); if (lane >= o) sc += t; }
;           const float b1 = sc, b0 = sc - f1, a0 = i0 - b0, a1 = i1 - b1;
;           float pm = fmaxf(a0, a1);
; #pragma unroll
;           for (int o = 1; o < 64; o <<= 1) { const float t = __shfl_up(pm, o); if (lane >= o) pm = fmaxf(pm, t); }
;           float pe = __shfl_up(pm, 1); if (lane == 0) pe = -3.0e38f;
;           sA[p0] = a0; sA[p0 + 1] = a1; sLF[p0] = b0; sLF[p0 + 1] = b1; sM[p0] = fmaxf(pe, a0); sM[p0 + 1] = pm; }
;       __syncthreads();
.LBB0_368:
	s_andn2_b64 vcc, exec, s[2:3]
	s_cbranch_vccnz .LBB0_438
	s_sub_i32 s98, 11, s93
	s_cmp_lt_u32 s93, 4
	s_cselect_b32 s98, s93, s98
	s_lshl_b32 s68, s98, 6
	s_lshl_b32 s44, s98, 4
	s_cmpk_gt_u32 s68, 0x7f
	s_cselect_b64 s[14:15], -1, 0
	s_cmpk_lt_u32 s68, 0x100
	s_cselect_b64 s[40:41], -1, 0
	s_cmpk_gt_u32 s68, 0xff
	s_cselect_b64 s[18:19], -1, 0
	s_cmpk_gt_u32 s68, 0x17f
	s_cselect_b64 s[20:21], -1, 0
	s_ashr_i32 s42, s33, 2
	s_ashr_i32 s43, s42, 31
	s_and_b32 s45, s33, 3
	s_lshl_b32 s4, s98, 8
	s_lshl_b64 s[2:3], s[42:43], 16
	v_and_b32_e32 v48, 63, v0
	v_or_b32_e32 v48, s68, v48
	s_add_u32 s2, s22, s2
	s_addc_u32 s3, s23, s3
	v_and_b32_e32 v49, 63, v48
	s_lshl_b32 s5, s45, 2
	v_lshl_or_b32 v2, v49, 1, s4
	s_add_u32 s2, s2, s5
	v_ashrrev_i32_e32 v3, 31, v2
	s_waitcnt vmcnt(6)
	v_or_b32_e32 v6, 0x80, v2
	s_addc_u32 s3, s3, 0
	v_lshlrev_b64 v[4:5], 5, v[2:3]
	v_ashrrev_i32_e32 v7, 31, v6
	v_lshl_add_u64 v[4:5], s[2:3], 0, v[4:5]
	v_lshlrev_b64 v[8:9], 5, v[6:7]
	s_barrier
	v_lshl_add_u64 v[8:9], s[2:3], 0, v[8:9]
	global_load_dword v1, v[4:5], off offset:16
	global_load_dword v3, v[4:5], off offset:48
	global_load_dword v7, v[8:9], off offset:16
	global_load_dword v12, v[8:9], off offset:48
	global_load_dword v10, v[4:5], off
	global_load_dword v11, v[4:5], off offset:32
	s_nop 0
	global_load_dword v4, v[8:9], off
	global_load_dword v5, v[8:9], off offset:32
	v_mbcnt_lo_u32_b32 v8, -1, 0
	v_mbcnt_hi_u32_b32 v46, -1, v8
	v_and_b32_e32 v47, 64, v46
	v_add_u32_e32 v8, -1, v46
	v_cmp_lt_i32_e32 vcc, v8, v47
	v_add_u32_e32 v9, -2, v46
	v_cmp_eq_u32_e64 s[2:3], 0, v49
	v_cndmask_b32_e32 v8, v8, v46, vcc
	s_waitcnt vmcnt(12)
	v_lshlrev_b32_e32 v17, 2, v8
	v_cmp_lt_i32_e32 vcc, v9, v47
	v_add_u32_e32 v13, -4, v46
	v_cmp_gt_u32_e64 s[4:5], 2, v49
	v_cndmask_b32_e32 v9, v9, v46, vcc
	s_waitcnt vmcnt(11)
	v_lshlrev_b32_e32 v19, 2, v9
	v_cmp_lt_i32_e32 vcc, v13, v47
	v_add_u32_e32 v14, -8, v46
	v_cmp_gt_u32_e64 s[6:7], 4, v49
	v_cndmask_b32_e32 v13, v13, v46, vcc
	v_cmp_lt_i32_e32 vcc, v14, v47
	v_add_u32_e32 v15, -16, v46
	v_cmp_gt_u32_e64 s[8:9], 8, v49
	v_subrev_u32_e32 v16, 32, v46
	v_cmp_gt_u32_e64 s[10:11], 32, v49
	v_lshlrev_b32_e32 v2, 2, v2
	s_add_i32 s22, 0, 0x17000
	v_add_u32_e32 v21, s22, v2
	v_lshlrev_b32_e32 v6, 2, v6
	s_waitcnt vmcnt(10)
	v_add_u32_e32 v22, s22, v6
	s_waitcnt vmcnt(6)
	v_add_f32_e32 v1, v1, v3
	ds_bpermute_b32 v8, v17, v1
	s_waitcnt vmcnt(4)
	v_add_f32_e32 v7, v7, v12
	ds_bpermute_b32 v18, v17, v7
	s_waitcnt lgkmcnt(1)
	v_add_f32_e32 v8, v1, v8
	v_cndmask_b32_e64 v1, v8, v1, s[2:3]
	s_waitcnt lgkmcnt(0)
	v_add_f32_e32 v9, v7, v18
	v_cndmask_b32_e64 v7, v9, v7, s[2:3]
	ds_bpermute_b32 v8, v19, v1
	ds_bpermute_b32 v9, v19, v7
	v_lshlrev_b32_e32 v18, 2, v13
	v_cndmask_b32_e32 v13, v14, v46, vcc
	v_lshlrev_b32_e32 v14, 2, v13
	s_waitcnt lgkmcnt(1)
	v_add_f32_e32 v8, v1, v8
	s_waitcnt lgkmcnt(0)
	v_add_f32_e32 v9, v7, v9
	v_cndmask_b32_e64 v1, v8, v1, s[4:5]
	v_cndmask_b32_e64 v7, v9, v7, s[4:5]
	ds_bpermute_b32 v8, v18, v1
	ds_bpermute_b32 v9, v18, v7
	v_cmp_lt_i32_e32 vcc, v15, v47
	s_waitcnt lgkmcnt(1)
	v_add_f32_e32 v8, v1, v8
	s_waitcnt lgkmcnt(0)
	v_add_f32_e32 v9, v7, v9
	v_cndmask_b32_e64 v1, v8, v1, s[6:7]
	v_cndmask_b32_e64 v7, v9, v7, s[6:7]
	ds_bpermute_b32 v8, v14, v1
	ds_bpermute_b32 v9, v14, v7
	v_cndmask_b32_e32 v13, v15, v46, vcc
	v_lshlrev_b32_e32 v15, 2, v13
	v_cmp_lt_i32_e32 vcc, v16, v47
	s_waitcnt lgkmcnt(1)
	v_add_f32_e32 v8, v1, v8
	s_waitcnt lgkmcnt(0)
	v_add_f32_e32 v9, v7, v9
	v_cndmask_b32_e64 v1, v8, v1, s[8:9]
	v_cndmask_b32_e64 v7, v9, v7, s[8:9]
	ds_bpermute_b32 v8, v15, v1
	ds_bpermute_b32 v9, v15, v7
	v_cndmask_b32_e32 v13, v16, v46, vcc
	v_cmp_gt_u32_e32 vcc, 16, v49
	v_lshlrev_b32_e32 v16, 2, v13
	s_waitcnt lgkmcnt(1)
	v_add_f32_e32 v8, v1, v8
	s_waitcnt lgkmcnt(0)
	v_add_f32_e32 v9, v7, v9
	v_cndmask_b32_e32 v1, v8, v1, vcc
	v_cndmask_b32_e32 v7, v9, v7, vcc
	ds_bpermute_b32 v8, v16, v1
	ds_bpermute_b32 v9, v16, v7
	s_waitcnt lgkmcnt(1)
	v_add_f32_e32 v8, v1, v8
	s_waitcnt lgkmcnt(0)
	v_add_f32_e32 v13, v7, v9
	v_cndmask_b32_e64 v9, v8, v1, s[10:11]
	v_cndmask_b32_e64 v13, v13, v7, s[10:11]
	v_sub_f32_e32 v8, v9, v3
	v_sub_f32_e32 v12, v13, v12
	s_waitcnt vmcnt(2)
	v_pk_add_f32 v[10:11], v[10:11], v[8:9] neg_lo:[0,1] neg_hi:[0,1]
	s_waitcnt vmcnt(0)
	v_pk_add_f32 v[4:5], v[4:5], v[12:13] neg_lo:[0,1] neg_hi:[0,1]
	v_max_f32_e32 v1, v10, v11
	v_max_f32_e32 v3, v4, v5
	ds_bpermute_b32 v7, v17, v1
	ds_bpermute_b32 v20, v17, v3
	s_waitcnt lgkmcnt(1)
	v_max_f32_e32 v7, v7, v7
	s_waitcnt lgkmcnt(0)
	v_max_f32_e32 v20, v20, v20
	v_max_f32_e32 v7, v1, v7
	v_max_f32_e32 v20, v3, v20
	v_cndmask_b32_e64 v1, v7, v1, s[2:3]
	v_cndmask_b32_e64 v3, v20, v3, s[2:3]
	ds_bpermute_b32 v7, v19, v1
	ds_bpermute_b32 v19, v19, v3
	v_mov_b32_e32 v20, 0xff61b1e6
	s_waitcnt lgkmcnt(1)
	v_max_f32_e32 v7, v7, v7
	s_waitcnt lgkmcnt(0)
	v_max_f32_e32 v19, v19, v19
	v_max_f32_e32 v7, v1, v7
	v_max_f32_e32 v19, v3, v19
	v_cndmask_b32_e64 v1, v7, v1, s[4:5]
	v_cndmask_b32_e64 v3, v19, v3, s[4:5]
	ds_bpermute_b32 v7, v18, v1
	ds_bpermute_b32 v18, v18, v3
	s_add_i32 s4, 0, 0x15000
	s_add_i32 s5, 0, 0x19000
	v_add_u32_e32 v19, s5, v2
	s_waitcnt lgkmcnt(1)
	v_max_f32_e32 v7, v7, v7
	s_waitcnt lgkmcnt(0)
	v_max_f32_e32 v18, v18, v18
	v_max_f32_e32 v7, v1, v7
	v_max_f32_e32 v18, v3, v18
	v_cndmask_b32_e64 v1, v7, v1, s[6:7]
	v_cndmask_b32_e64 v3, v18, v3, s[6:7]
	ds_bpermute_b32 v7, v14, v1
	ds_bpermute_b32 v14, v14, v3
	v_add_u32_e32 v18, s4, v2
	ds_write_b64 v19, v[8:9]
	s_waitcnt lgkmcnt(2)
	v_max_f32_e32 v2, v7, v7
	s_waitcnt lgkmcnt(1)
	v_max_f32_e32 v7, v14, v14
	v_max_f32_e32 v2, v1, v2
	v_max_f32_e32 v7, v3, v7
	v_cndmask_b32_e64 v1, v2, v1, s[8:9]
	v_cndmask_b32_e64 v2, v7, v3, s[8:9]
	ds_bpermute_b32 v3, v15, v1
	ds_bpermute_b32 v7, v15, v2
	v_add_u32_e32 v14, s4, v6
	v_add_u32_e32 v15, s5, v6
	ds_write_b64 v15, v[12:13]
	ds_write_b64 v18, v[10:11]
	ds_write_b64 v14, v[4:5]
	s_waitcnt lgkmcnt(4)
	v_max_f32_e32 v3, v3, v3
	s_waitcnt lgkmcnt(3)
	v_max_f32_e32 v6, v7, v7
	v_max_f32_e32 v3, v1, v3
	v_max_f32_e32 v6, v2, v6
	v_cndmask_b32_e32 v1, v3, v1, vcc
	v_cndmask_b32_e32 v2, v6, v2, vcc
	ds_bpermute_b32 v3, v16, v1
	ds_bpermute_b32 v6, v16, v2
	v_max_f32_e32 v7, v1, v1
	v_max_f32_e32 v8, v2, v2
	s_waitcnt lgkmcnt(1)
	v_max_f32_e32 v3, v3, v3
	s_waitcnt lgkmcnt(0)
	v_max_f32_e32 v6, v6, v6
	v_max_f32_e32 v3, v7, v3
	v_max_f32_e32 v6, v8, v6
	v_cndmask_b32_e64 v3, v3, v1, s[10:11]
	v_cndmask_b32_e64 v7, v6, v2, s[10:11]
	ds_bpermute_b32 v1, v17, v3
	ds_bpermute_b32 v2, v17, v7
	s_waitcnt lgkmcnt(1)
	v_cndmask_b32_e64 v1, v1, v20, s[2:3]
	s_waitcnt lgkmcnt(0)
	v_cndmask_b32_e64 v2, v2, v20, s[2:3]
	v_max_f32_e32 v1, v1, v1
	v_max_f32_e32 v5, v2, v2
	v_max_f32_e32 v2, v1, v10
	v_cmp_eq_u32_e64 s[2:3], 0, v48
	v_max_f32_e32 v6, v5, v4
	ds_write_b64 v21, v[2:3]
	ds_write_b64 v22, v[6:7]
	s_waitcnt lgkmcnt(0)
	s_barrier
; __device__ __forceinline__ void p2_mlstm_chain(Frame& F, const Args& A, int ch) {
;     ...
;       if (tid == 0) { float m = 0.f; for (int c = 0; c < 16; ++c) { sMC[c] = m; const float Mn = fmaxf(m, sM[c * 128 + 127]); sMC[32 + c] = Mn; m = sLF[c * 128 + 127] + Mn; } sMC[16] = m; }
	s_and_saveexec_b64 s[4:5], s[2:3]
	s_cbranch_execz .LBB0_371
	s_add_i32 s2, 0, 0x171fc
	v_mov_b32_e32 v1, s2
	s_add_i32 s2, 0, 0x191fc
	v_mov_b32_e32 v2, s2
	s_add_i32 s2, 0, 0x173fc
	v_mov_b32_e32 v3, s2
	s_add_i32 s2, 0, 0x193fc
	v_mov_b32_e32 v4, s2
	s_add_i32 s2, 0, 0x175fc
	v_mov_b32_e32 v5, s2
	s_add_i32 s2, 0, 0x195fc
	v_mov_b32_e32 v6, s2
	s_add_i32 s2, 0, 0x177fc
	v_mov_b32_e32 v7, s2
	s_add_i32 s2, 0, 0x197fc
	v_mov_b32_e32 v8, s2
	ds_read_b32 v1, v1
	ds_read_b32 v9, v2
	ds_read_b32 v3, v3
	ds_read_b32 v4, v4
	ds_read_b32 v5, v5
	ds_read_b32 v6, v6
	ds_read_b32 v10, v7
	ds_read_b32 v11, v8
	s_waitcnt lgkmcnt(7)
	v_max_f32_e32 v1, v1, v1
	v_max_f32_e32 v2, 0, v1
	s_waitcnt lgkmcnt(6)
	v_add_f32_e32 v7, v2, v9
	s_waitcnt lgkmcnt(5)
	v_max_f32_e32 v1, v3, v3
	v_max_f32_e32 v3, v7, v1
	s_waitcnt lgkmcnt(4)
	v_add_f32_e32 v8, v3, v4
	s_waitcnt lgkmcnt(3)
	v_max_f32_e32 v1, v5, v5
	v_max_f32_e32 v4, v8, v1
	s_add_i32 s2, 0, 0x1b000
	s_waitcnt lgkmcnt(2)
	v_add_f32_e32 v9, v4, v6
	v_mov_b32_e32 v6, 0
	v_mov_b32_e32 v1, s2
	ds_write_b128 v1, v[6:9]
	s_waitcnt lgkmcnt(2)
	v_max_f32_e32 v1, v10, v10
	s_add_i32 s2, 0, 0x1b080
	v_max_f32_e32 v5, v9, v1
	v_mov_b32_e32 v1, s2
	s_add_i32 s2, 0, 0x179fc
	ds_write_b128 v1, v[2:5]
	v_mov_b32_e32 v1, s2
	s_add_i32 s2, 0, 0x199fc
	v_mov_b32_e32 v3, s2
	s_add_i32 s2, 0, 0x17bfc
	v_mov_b32_e32 v4, s2
	s_add_i32 s2, 0, 0x19bfc
	s_waitcnt lgkmcnt(2)
	v_add_f32_e32 v2, v5, v11
	v_mov_b32_e32 v5, s2
	s_add_i32 s2, 0, 0x17dfc
	v_mov_b32_e32 v6, s2
	s_add_i32 s2, 0, 0x19dfc
	v_mov_b32_e32 v7, s2
	s_add_i32 s2, 0, 0x17ffc
	v_mov_b32_e32 v8, s2
	s_add_i32 s2, 0, 0x19ffc
	v_mov_b32_e32 v9, s2
	ds_read_b32 v1, v1
	ds_read_b32 v3, v3
	ds_read_b32 v4, v4
	ds_read_b32 v5, v5
	ds_read_b32 v10, v6
	ds_read_b32 v11, v7
	ds_read_b32 v12, v8
	ds_read_b32 v13, v9
	s_waitcnt lgkmcnt(7)
	v_max_f32_e32 v1, v1, v1
	v_max_f32_e32 v6, v2, v1
	s_waitcnt lgkmcnt(6)
	v_add_f32_e32 v3, v6, v3
	s_waitcnt lgkmcnt(5)
	v_max_f32_e32 v1, v4, v4
	v_max_f32_e32 v7, v3, v1
	s_waitcnt lgkmcnt(4)
	v_add_f32_e32 v4, v7, v5
	s_waitcnt lgkmcnt(3)
	v_max_f32_e32 v1, v10, v10
	v_max_f32_e32 v8, v4, v1
	s_add_i32 s2, 0, 0x1b010
	s_waitcnt lgkmcnt(2)
	v_add_f32_e32 v5, v8, v11
	v_mov_b32_e32 v1, s2
	ds_write_b128 v1, v[2:5]
	s_waitcnt lgkmcnt(2)
	v_max_f32_e32 v1, v12, v12
	s_add_i32 s2, 0, 0x1b090
	v_max_f32_e32 v9, v5, v1
	v_mov_b32_e32 v1, s2
	s_add_i32 s2, 0, 0x181fc
	ds_write_b128 v1, v[6:9]
	v_mov_b32_e32 v1, s2
	s_add_i32 s2, 0, 0x1a1fc
	v_mov_b32_e32 v3, s2
	s_add_i32 s2, 0, 0x183fc
	v_mov_b32_e32 v4, s2
	s_add_i32 s2, 0, 0x1a3fc
	v_mov_b32_e32 v5, s2
	s_add_i32 s2, 0, 0x185fc
	v_mov_b32_e32 v6, s2
	s_add_i32 s2, 0, 0x1a5fc
	v_mov_b32_e32 v7, s2
	s_add_i32 s2, 0, 0x187fc
	v_mov_b32_e32 v8, s2
	s_add_i32 s2, 0, 0x1a7fc
	s_waitcnt lgkmcnt(2)
	v_add_f32_e32 v2, v9, v13
	v_mov_b32_e32 v9, s2
	ds_read_b32 v1, v1
	ds_read_b32 v3, v3
	ds_read_b32 v4, v4
	ds_read_b32 v5, v5
	ds_read_b32 v10, v6
	ds_read_b32 v11, v7
	ds_read_b32 v12, v8
	ds_read_b32 v13, v9
	s_waitcnt lgkmcnt(7)
	v_max_f32_e32 v1, v1, v1
	v_max_f32_e32 v6, v2, v1
	s_waitcnt lgkmcnt(6)
	v_add_f32_e32 v3, v6, v3
	s_waitcnt lgkmcnt(5)
	v_max_f32_e32 v1, v4, v4
	v_max_f32_e32 v7, v3, v1
	s_waitcnt lgkmcnt(4)
	v_add_f32_e32 v4, v7, v5
	s_waitcnt lgkmcnt(3)
	v_max_f32_e32 v1, v10, v10
	v_max_f32_e32 v8, v4, v1
	s_add_i32 s2, 0, 0x1b020
	s_waitcnt lgkmcnt(2)
	v_add_f32_e32 v5, v8, v11
	v_mov_b32_e32 v1, s2
	ds_write_b128 v1, v[2:5]
	s_waitcnt lgkmcnt(2)
	v_max_f32_e32 v1, v12, v12
	s_add_i32 s2, 0, 0x1b0a0
	v_max_f32_e32 v9, v5, v1
	v_mov_b32_e32 v1, s2
	s_add_i32 s2, 0, 0x189fc
	ds_write_b128 v1, v[6:9]
	v_mov_b32_e32 v1, s2
	s_add_i32 s2, 0, 0x1a9fc
	v_mov_b32_e32 v3, s2
	s_add_i32 s2, 0, 0x18bfc
	v_mov_b32_e32 v4, s2
	s_add_i32 s2, 0, 0x1abfc
	v_mov_b32_e32 v5, s2
	s_add_i32 s2, 0, 0x18dfc
	v_mov_b32_e32 v6, s2
	s_add_i32 s2, 0, 0x1adfc
	v_mov_b32_e32 v7, s2
	s_add_i32 s2, 0, 0x18ffc
	v_mov_b32_e32 v8, s2
	s_add_i32 s2, 0, 0x1affc
	s_waitcnt lgkmcnt(2)
	v_add_f32_e32 v2, v9, v13
	v_mov_b32_e32 v9, s2
	ds_read_b32 v1, v1
	ds_read_b32 v3, v3
	ds_read_b32 v4, v4
	ds_read_b32 v5, v5
	ds_read_b32 v10, v6
	ds_read_b32 v11, v7
	ds_read_b32 v12, v8
	ds_read_b32 v13, v9
	s_waitcnt lgkmcnt(7)
	v_max_f32_e32 v1, v1, v1
	v_max_f32_e32 v6, v2, v1
	s_waitcnt lgkmcnt(6)
	v_add_f32_e32 v3, v6, v3
	s_waitcnt lgkmcnt(5)
	v_max_f32_e32 v1, v4, v4
	v_max_f32_e32 v7, v3, v1
	s_waitcnt lgkmcnt(4)
	v_add_f32_e32 v4, v7, v5
	s_waitcnt lgkmcnt(3)
	v_max_f32_e32 v1, v10, v10
	v_max_f32_e32 v8, v4, v1
	s_add_i32 s2, 0, 0x1b030
	s_waitcnt lgkmcnt(2)
	v_add_f32_e32 v5, v8, v11
	v_mov_b32_e32 v1, s2
	ds_write_b128 v1, v[2:5]
	s_waitcnt lgkmcnt(2)
	v_max_f32_e32 v1, v12, v12
	s_add_i32 s2, 0, 0x1b0b0
	v_max_f32_e32 v9, v5, v1
	v_mov_b32_e32 v1, s2
	s_add_i32 s2, 0, 0x1b040
	ds_write_b128 v1, v[6:9]
	s_waitcnt lgkmcnt(2)
	v_add_f32_e32 v1, v9, v13
	v_mov_b32_e32 v2, s2
	ds_write_b32 v2, v1

; #define GAS __attribute__((address_space(1)))
; #define LAS __attribute__((address_space(3)))
; __device__ __forceinline__ void p2_mlstm_chain(Frame& F, const Args& A, int ch) {
;     ...
;       if (tid < 64) ns[tid] = 0.f;
;       __syncthreads(); }
;     f32x4 Cst[4]; f32x4 Nst = (f32x4){0.f, 0.f, 0.f, 0.f};
; #pragma unroll
;     for (int i = 0; i < 4; ++i) Cst[i] = (f32x4){0.f, 0.f, 0.f, 0.f};
;     u32x4 qreg[2], kreg[2], vreg[4];
;     { const size_t tg0 = (size_t)b * SEQ;
; #pragma unroll
;       for (int j = 0; j < 2; ++j) { const int idx = tid + 512 * j, row = idx >> 3, part = idx & 7; const bf16* src = proj + (tg0 + row) * NP + h * 64 + part * 8; qreg[j] = *(const GAS u32x4*)src; kreg[j] = *(const GAS u32x4*)(src + 256); }
; #pragma unroll
;       for (int j = 0; j < 4; ++j) { const int idx = tid + 512 * j, row = idx >> 4, part = idx & 15; vreg[j] = *(const GAS u32x4*)(proj + (tg0 + row) * NP + 512 + h * 128 + part * 8); } }
; #pragma unroll 1
;     for (int c = 0; c < 16; ++c) {
;         const size_t tg0 = (size_t)b * SEQ + c * 128; const int t = 16 * w + tl;
; #pragma unroll
;         for (int j = 0; j < 2; ++j) { const int idx = tid + 512 * j, row = idx >> 3, part = idx & 7; *(LAS u32x4*)(L + ML_QS + row * 144 + part * 16) = qreg[j];
;             *(LAS u32x4*)(L + ML_KS + 128 * row + 32 * ((part >> 1) ^ swzg(row)) + 16 * (part & 1)) = kreg[j]; }
; #pragma unroll
;         for (int j = 0; j < 4; ++j) { const int idx = tid + 512 * j, row = idx >> 4, part = idx & 15; *(LAS u32x4*)(L + ML_VS + 256 * row + 32 * ((part >> 1) ^ swzf(row)) + 16 * (part & 1)) = vreg[j]; }
;         const float mc = sMC[c], Mn = sMC[32 + c], Mt = sM[c * 128 + t], lf = sLF[c * 128 + t];
;         if (tid < 128) sWK[tid] = __builtin_amdgcn_exp2f((sA[c * 128 + tid] - Mn) * 1.4426950408889634f);
;     ...
;           for (int st = 0; st < 4; ++st) { const f32x4 k0 = *(const LAS f32x4*)(sWK + 32 * st + 8 * fq), k1 = *(const LAS f32x4*)(sWK + 32 * st + 8 * fq + 4);
;               const bf16x8 a = scale_frag8(tr_frag_V(L + ML_VS, 32 * st + 8 * fq, 32 * st + 8 * fq + 4, w, tl), k0, k1);
;               const u32x4 wkp = (u32x4){cvt_pk_bf16(k0[0], k0[1]), cvt_pk_bf16(k0[2], k0[3]), cvt_pk_bf16(k1[0], k1[1]), cvt_pk_bf16(k1[2], k1[3])};
;               const bf16x8 an = __builtin_bit_cast(bf16x8, tl == 0 ? wkp : (u32x4){0u, 0u, 0u, 0u});
; #pragma unroll
.LBB0_374:
	v_writelane_b32 v254, s72, 8
	s_nop 1
	v_writelane_b32 v254, s73, 9
	s_or_b64 exec, exec, s[4:5]
	v_cmp_gt_i32_e64 s[2:3], 64, v48
	s_and_saveexec_b64 s[4:5], s[2:3]
	v_add_u32_e32 v2, 0x14800, v2
	v_mov_b32_e32 v3, 0
	ds_write_b32 v2, v3
	s_or_b64 exec, exec, s[4:5]
	s_lshl_b32 s60, s45, 7
	s_lshl_b32 s2, s45, 9
	s_add_u32 s4, s26, s2
	s_addc_u32 s5, s27, 0
	s_lshl_b64 s[2:3], s[42:43], 11
	s_add_u32 s6, s12, s60
	s_addc_u32 s7, s13, 0
	s_cmp_lt_u32 s68, 64
	s_cselect_b64 s[24:25], -1, 0
	s_cmp_gt_u32 s68, 63
	s_cselect_b64 s[26:27], -1, 0
	s_cmpk_gt_u32 s68, 0xbf
	s_cselect_b64 s[28:29], -1, 0
	s_cmpk_gt_u32 s68, 0x13f
	s_cselect_b64 s[30:31], -1, 0
	s_cmpk_gt_u32 s68, 0x1bf
	v_ashrrev_i32_e32 v38, 4, v48
	s_cselect_b64 s[82:83], -1, 0
	s_cmp_eq_u32 s98, 1
	v_lshlrev_b32_e32 v50, 4, v48
	v_ashrrev_i32_e32 v39, 31, v38
	s_cselect_b64 s[34:35], -1, 0
	s_cmp_eq_u32 s98, 2
	v_and_b32_e32 v106, 0x70, v50
	v_mov_b32_e32 v107, 0
	s_movk_i32 s46, 0x1400
	v_lshl_add_u64 v[20:21], s[2:3], 0, v[38:39]
	v_mov_b64_e32 v[28:29], s[12:13]
	v_ashrrev_i32_e32 v40, 4, v18
	v_ashrrev_i32_e32 v42, 4, v1
	v_ashrrev_i32_e32 v44, 4, v26
	v_lshrrev_b32_e32 v52, 4, v49
	s_cselect_b64 s[36:37], -1, 0
	s_cmp_eq_u32 s98, 3
	v_lshl_add_u64 v[10:11], s[6:7], 0, v[106:107]
	v_ashrrev_i32_e32 v34, 3, v48
	v_ashrrev_i32_e32 v36, 3, v18
	v_mad_u64_u32 v[22:23], s[6:7], v20, s46, v[28:29]
	v_ashrrev_i32_e32 v41, 31, v40
	v_ashrrev_i32_e32 v43, 31, v42
	v_ashrrev_i32_e32 v45, 31, v44
	s_mov_b32 s23, 0
	s_cselect_b64 s[38:39], -1, 0
	v_lshlrev_b32_e32 v53, 3, v48
	v_ashrrev_i32_e32 v35, 31, v34
	v_ashrrev_i32_e32 v37, 31, v36
	v_mad_i32_i24 v23, v21, s46, v23
	s_lshl_b32 s22, s45, 8
	v_lshl_add_u64 v[18:19], s[2:3], 0, v[40:41]
	v_lshl_add_u64 v[30:31], s[2:3], 0, v[42:43]
	v_lshl_add_u64 v[26:27], s[2:3], 0, v[44:45]
	v_lshlrev_b32_e32 v68, 2, v52
	v_lshlrev_b32_e32 v146, 5, v52
	v_lshlrev_b32_e32 v39, 3, v52
	v_lshlrev_b32_e32 v52, 1, v52
	v_lshl_add_u64 v[2:3], s[2:3], 0, v[34:35]
	v_lshl_add_u64 v[12:13], s[2:3], 0, v[36:37]
	v_lshl_add_u64 v[20:21], v[22:23], 0, s[22:23]
	v_mad_u64_u32 v[22:23], s[6:7], v18, s46, v[28:29]
	v_mad_u64_u32 v[32:33], s[6:7], v30, s46, v[28:29]
	v_mad_u64_u32 v[28:29], s[2:3], v26, s46, v[28:29]
	v_lshrrev_b32_e32 v37, 1, v48
	v_bfe_u32 v70, v48, 2, 2
	v_and_b32_e32 v43, 24, v53
	v_xor_b32_e32 v53, v52, v68
	v_mad_i32_i24 v23, v19, s46, v23
	v_mad_i32_i24 v33, v31, s46, v33
	v_mad_i32_i24 v29, v27, s46, v29
	v_and_or_b32 v74, v53, 4, v70
	v_and_b32_e32 v77, 2, v52
	v_and_b32_e32 v52, 3, v48
	v_bitop3_b32 v37, v37, 4, v48 bitop3:0x48
	v_lshrrev_b32_e32 v53, 2, v34
	v_and_b32_e32 v64, 15, v48
	v_and_b32_e32 v106, 0xf0, v50
	v_lshl_add_u64 v[18:19], v[22:23], 0, s[22:23]
	v_lshl_add_u64 v[30:31], v[32:33], 0, s[22:23]
	v_lshl_add_u64 v[26:27], v[28:29], 0, s[22:23]
	v_bfe_u32 v35, v48, 1, 2
	v_bitop3_b32 v37, v37, s98, v52 bitop3:0x36
	v_bfe_u32 v52, v34, 1, 1
	v_and_b32_e32 v53, 2, v53
	v_lshrrev_b32_e32 v59, 2, v36
	v_lshl_add_u64 v[20:21], v[20:21], 0, v[106:107]
	v_lshl_add_u64 v[22:23], v[18:19], 0, v[106:107]
	v_lshl_add_u64 v[30:31], v[30:31], 0, v[106:107]
	v_lshl_add_u64 v[32:33], v[26:27], 0, v[106:107]
	v_lshrrev_b32_e32 v58, 5, v49
	s_add_i32 s8, 0, 0x10800
	v_and_b32_e32 v106, 48, v49
	v_lshlrev_b32_e32 v49, 8, v64
	v_lshlrev_b32_e32 v37, 5, v37
	v_bitop3_b32 v52, v52, v35, v53 bitop3:0x36
	v_bfe_u32 v57, v36, 1, 1
	v_and_b32_e32 v59, 2, v59
	v_add3_u32 v49, s8, v49, v37
	v_lshlrev_b32_e32 v37, 7, v34
	v_lshlrev_b32_e32 v52, 5, v52
	v_bitop3_b32 v35, v57, v35, v59 bitop3:0x36
	v_add3_u32 v52, 0, v37, v52
	v_lshlrev_b32_e32 v37, 7, v36
	v_lshlrev_b32_e32 v35, 5, v35
	v_lshrrev_b32_e32 v59, 1, v38
	v_bfe_u32 v55, v48, 1, 3
	v_add3_u32 v57, 0, v37, v35
	v_and_b32_e32 v37, 3, v38
	v_bitop3_b32 v59, v59, 4, v38 bitop3:0x48
	v_mad_u64_u32 v[6:7], s[6:7], v2, s46, v[10:11]
	v_mad_u64_u32 v[14:15], s[6:7], v12, s46, v[10:11]
	v_bitop3_b32 v37, v59, v55, v37 bitop3:0x36
	v_mad_i32_i24 v7, v3, s46, v7
	v_mad_i32_i24 v15, v13, s46, v15
	v_lshlrev_b32_e32 v35, 8, v38
	v_lshlrev_b32_e32 v37, 5, v37
	v_lshrrev_b32_e32 v60, 1, v40
	s_waitcnt lgkmcnt(0)
	s_barrier
	global_load_dwordx4 v[2:5], v[6:7], off
	s_nop 0
	global_load_dwordx4 v[6:9], v[6:7], off offset:512
	s_nop 0
	global_load_dwordx4 v[10:13], v[14:15], off
	s_nop 0
	global_load_dwordx4 v[14:17], v[14:15], off offset:512
	s_nop 0
	global_load_dwordx4 v[18:21], v[20:21], off offset:1024
	s_nop 0
	global_load_dwordx4 v[22:25], v[22:23], off offset:1024
	s_nop 0
	global_load_dwordx4 v[26:29], v[30:31], off offset:1024
	s_nop 0
	global_load_dwordx4 v[30:33], v[32:33], off offset:1024
	v_add3_u32 v59, 0, v35, v37
	v_and_b32_e32 v37, 3, v40
	v_bitop3_b32 v60, v60, 4, v40 bitop3:0x48
	v_bitop3_b32 v37, v60, v55, v37 bitop3:0x36
	v_lshlrev_b32_e32 v35, 8, v40
	v_lshlrev_b32_e32 v37, 5, v37
	v_lshrrev_b32_e32 v61, 1, v42
	v_add3_u32 v60, 0, v35, v37
	v_and_b32_e32 v37, 3, v42
	v_bitop3_b32 v61, v61, 4, v42 bitop3:0x48
	v_bitop3_b32 v37, v61, v55, v37 bitop3:0x36
	v_lshlrev_b32_e32 v35, 8, v42
	v_lshlrev_b32_e32 v37, 5, v37
	v_lshrrev_b32_e32 v62, 1, v44
	v_or_b32_e32 v54, s44, v64
	v_and_b32_e32 v1, 7, v48
	s_movk_i32 s6, 0x90
	v_add3_u32 v61, 0, v35, v37
	v_and_b32_e32 v37, 3, v44
	v_bitop3_b32 v62, v62, 4, v44 bitop3:0x48
	v_lshlrev_b32_e32 v63, 4, v1
	v_mul_lo_u32 v1, v54, s6
	v_bitop3_b32 v37, v62, v55, v37 bitop3:0x36
	v_and_b32_e32 v41, 16, v50
	v_add_u32_e32 v50, 0, v1
	v_lshrrev_b32_e32 v1, 2, v48
	v_lshlrev_b32_e32 v35, 8, v44
	v_lshlrev_b32_e32 v37, 5, v37
	v_bfe_u32 v56, v48, 1, 1
	v_and_b32_e32 v66, 2, v1
	v_and_b32_e32 v69, 16, v48
	v_add3_u32 v62, 0, v35, v37
; #define LAS __attribute__((address_space(3)))
; __device__ __forceinline__ unsigned cvt_pk_bf16(float lo, float hi) { unsigned r; asm volatile("v_cvt_pk_bf16_f32 %0, %1, %2" : "=v"(r) : "v"(lo), "v"(hi)); return r; }
; __device__ __forceinline__ void p2_mlstm_chain(Frame& F, const Args& A, int ch) {
;     ...
;         for (int sb = 0; sb < 8; ++sb) {
;             if (sb <= w) {
;                 f32x4 G = (f32x4){0.f, 0.f, 0.f, 0.f}; const int sr = 16 * sb + tl;
; #pragma unroll
;                 for (int ds = 0; ds < 2; ++ds) { const bf16x8 a = *(const LAS bf16x8*)(L + ML_KS + 128 * sr + 32 * ((2 * ds + (fq >> 1)) ^ swzg(sr)) + 16 * (fq & 1)); G = __builtin_amdgcn_mfma_f32_16x16x32_bf16(a, qf[ds], G, 0, 0, 0); }
;                 const f32x4 as = *(const LAS f32x4*)(sA + c * 128 + 16 * sb + 4 * fq);
;                 float sw[4];
; #pragma unroll
;                 for (int r = 0; r < 4; ++r) { const int s = 16 * sb + 4 * fq + r; float wg = __builtin_amdgcn_exp2f((as[r] - Mt) * 1.4426950408889634f) * 0.125f; if (s > t) wg = 0.f; sw[r] = G[r] * wg; den += sw[r]; }
;                 sfr[sb >> 1][(sb & 1) * 2] = cvt_pk_bf16(sw[0], sw[1]); sfr[sb >> 1][(sb & 1) * 2 + 1] = cvt_pk_bf16(sw[2], sw[3]);
;             }
;     ...
;           for (int st = 0; st < 4; ++st) { const f32x4 k0 = *(const LAS f32x4*)(sWK + 32 * st + 8 * fq), k1 = *(const LAS f32x4*)(sWK + 32 * st + 8 * fq + 4);
;               const bf16x8 a = scale_frag8(tr_frag_V(L + ML_VS, 32 * st + 8 * fq, 32 * st + 8 * fq + 4, w, tl), k0, k1);
;               const u32x4 wkp = (u32x4){cvt_pk_bf16(k0[0], k0[1]), cvt_pk_bf16(k0[2], k0[3]), cvt_pk_bf16(k1[0], k1[1]), cvt_pk_bf16(k1[2], k1[3])};
;               const bf16x8 an = __builtin_bit_cast(bf16x8, tl == 0 ? wkp : (u32x4){0u, 0u, 0u, 0u});
; #pragma unroll
;               for (int db = 0; db < 4; ++db) { const bf16x8 bb = tr_frag_K(L + ML_KS, 32 * st + 8 * fq, 32 * st + 8 * fq + 4, db, tl); Cst[db] = __builtin_amdgcn_mfma_f32_16x16x32_bf16(a, bb, Cst[db], 0, 0, 0);
;                   if (db == w) Nst = __builtin_amdgcn_mfma_f32_16x16x32_bf16(an, bb, Nst, 0, 0, 0); } } }
;         __syncthreads();
; #pragma unroll
;         for (int db = 0; db < 4; ++db) { const int d = 16 * db + tl; *(LAS u32x2*)(L + ML_CT + 256 * d + 32 * (w ^ swzf(d)) + 8 * fq) = (u32x2){cvt_pk_bf16(Cst[db][0], Cst[db][1]), cvt_pk_bf16(Cst[db][2], Cst[db][3])}; }
	v_lshlrev_b32_e32 v35, 7, v64
	v_or_b32_e32 v67, v56, v66
	v_add3_u32 v55, 0, v69, v35
	v_bitop3_b32 v35, v56, v58, v66 bitop3:0x36
	v_lshlrev_b32_e32 v56, 5, v35
	v_bitop3_b32 v35, v58, v67, 2 bitop3:0x36
	v_lshlrev_b32_e32 v58, 5, v35
	v_or_b32_e32 v35, 3, v68
	v_cmp_gt_u32_e64 s[10:11], v35, v54
	v_or_b32_e32 v35, 17, v68
	v_or_b32_e32 v37, 2, v68
	v_cmp_gt_u32_e64 s[48:49], v35, v54
	v_cmp_gt_u32_e64 s[12:13], v37, v54
	v_or_b32_e32 v37, 16, v68
	v_writelane_b32 v254, s48, 10
	v_or_b32_e32 v35, 19, v68
	v_xor_b32_e32 v66, 16, v46
	v_writelane_b32 v254, s49, 11
	v_cmp_gt_u32_e64 s[48:49], v37, v54
	v_or_b32_e32 v37, 18, v68
	v_add_u32_e32 v47, 64, v47
	v_writelane_b32 v254, s48, 12
	s_and_b64 s[40:41], s[40:41], vcc
	v_cmp_lt_i32_e32 vcc, v66, v47
	v_writelane_b32 v254, s49, 13
	v_cmp_gt_u32_e64 s[48:49], v35, v54
	v_or_b32_e32 v35, 33, v68
	v_cndmask_b32_e32 v69, v46, v66, vcc
	v_writelane_b32 v254, s48, 14
	v_xor_b32_e32 v66, 32, v46
	v_cmp_lt_i32_e32 vcc, v66, v47
	v_writelane_b32 v254, s49, 15
	v_cmp_gt_u32_e64 s[48:49], v37, v54
	v_or_b32_e32 v37, 32, v68
	v_cndmask_b32_e32 v79, v46, v66, vcc
	v_writelane_b32 v254, s48, 16
	v_add_u32_e32 v46, s44, v64
	v_mov_b32_e32 v47, v107
	v_writelane_b32 v254, s49, 17
	v_cmp_gt_u32_e64 s[48:49], v35, v54
	v_or_b32_e32 v35, 35, v68
	v_and_b32_e32 v51, 48, v48
	v_writelane_b32 v254, s48, 18
	v_lshlrev_b64 v[66:67], 11, v[46:47]
	v_lshrrev_b32_e32 v81, 1, v51
	v_writelane_b32 v254, s49, 19
	v_cmp_gt_u32_e64 s[48:49], v37, v54
	v_or_b32_e32 v37, 34, v68
	s_mov_b64 s[44:45], 0x5000080
	v_writelane_b32 v254, s48, 20
	v_mov_b32_e32 v80, 0xa00000
	v_or_b32_e32 v76, 4, v70
	v_writelane_b32 v254, s49, 21
	v_cmp_gt_u32_e64 s[48:49], v35, v54
	v_or_b32_e32 v35, 49, v68
	v_or_b32_e32 v87, v39, v76
	v_writelane_b32 v254, s48, 22
	v_lshrrev_b32_e32 v89, 1, v87
	v_and_b32_e32 v90, 4, v89
	v_writelane_b32 v254, s49, 23
	v_cmp_gt_u32_e64 s[48:49], v37, v54
	v_or_b32_e32 v37, 48, v68
	v_bitop3_b32 v90, v90, s98, v70 bitop3:0x36
	v_writelane_b32 v254, s48, 24
	v_lshlrev_b32_e32 v90, 5, v90
	v_lshlrev_b32_e32 v88, 8, v87
	v_writelane_b32 v254, s49, 25
	v_cmp_gt_u32_e64 s[48:49], v35, v54
	v_or_b32_e32 v35, 51, v68
	v_xor_b32_e32 v90, 0x80, v90
	v_writelane_b32 v254, s48, 26
	v_add3_u32 v88, 0, v90, v88
	v_and_b32_e32 v71, 4, v68
	v_writelane_b32 v254, s49, 27
	v_cmp_gt_u32_e64 s[48:49], v37, v54
	v_or_b32_e32 v37, 50, v68
	v_or_b32_e32 v72, v71, v70
	v_writelane_b32 v254, s48, 28
	s_movk_i32 s22, 0x80
	v_add_u32_e32 v73, s8, v43
	v_writelane_b32 v254, s49, 29
	v_cmp_gt_u32_e64 s[48:49], v35, v54
	v_or_b32_e32 v35, 0x41, v68
	v_cmp_gt_i32_e64 s[2:3], s22, v48
	v_writelane_b32 v254, s48, 30
	v_lshlrev_b32_e32 v65, 2, v48
	v_lshrrev_b32_e32 v78, 3, v48
	v_writelane_b32 v254, s49, 31
	v_cmp_gt_u32_e64 s[48:49], v37, v54
	v_or_b32_e32 v37, 64, v68
	v_mul_lo_u32 v48, v34, s6
	v_writelane_b32 v254, s48, 32
	v_mul_lo_u32 v53, v36, s6
	v_bitop3_b32 v71, v71, s98, v70 bitop3:0x36
	v_writelane_b32 v254, s49, 33
	v_cmp_gt_u32_e64 s[48:49], v35, v54
	v_or_b32_e32 v35, 0x43, v68
	v_add_u32_e32 v75, 0, v43
	v_writelane_b32 v254, s48, 34
	v_lshl_add_u32 v71, v71, 5, 0
	s_add_i32 s7, 0, 0x14a00
	v_writelane_b32 v254, s49, 35
	v_cmp_gt_u32_e64 s[48:49], v37, v54
	v_or_b32_e32 v37, 0x42, v68
	v_and_or_b32 v78, v78, 1, v77
	v_writelane_b32 v254, s48, 36
	v_add_u32_e32 v1, s7, v65
	v_add_u32_e32 v147, s7, v146
	v_writelane_b32 v254, s49, 37
	s_lshl_b64 s[48:49], s[42:43], 22
	s_lshl_b32 s43, s33, 8
	v_lshl_add_u64 v[66:67], s[48:49], 0, v[66:67]
	s_and_b32 s50, s43, 0x300
	v_or3_b32 v66, v66, s50, v81
	v_lshl_add_u64 v[66:67], s[58:59], 0, v[66:67]
	v_lshl_add_u64 v[110:111], v[66:67], 0, s[44:45]
	v_mad_i64_i32 v[66:67], s[44:45], v38, s46, 0
	v_mad_i64_i32 v[66:67], s[44:45], s42, v80, v[66:67]
	v_lshlrev_b32_e32 v38, 4, v64
	v_or3_b32 v66, v66, s50, v38
	v_lshl_add_u64 v[66:67], s[58:59], 0, v[66:67]
	s_mov_b64 s[44:45], 0x270a0400
	v_lshl_add_u64 v[112:113], v[66:67], 0, s[44:45]
	v_mad_i64_i32 v[66:67], s[48:49], v40, s46, 0
	v_mad_i64_i32 v[66:67], s[48:49], s42, v80, v[66:67]
	v_or3_b32 v66, v66, s50, v38
	v_lshl_add_u64 v[66:67], s[58:59], 0, v[66:67]
	v_lshl_add_u64 v[114:115], v[66:67], 0, s[44:45]
	v_mad_i64_i32 v[66:67], s[48:49], v42, s46, 0
	v_mad_i64_i32 v[66:67], s[48:49], s42, v80, v[66:67]
	v_or3_b32 v66, v66, s50, v38
	v_lshl_add_u64 v[66:67], s[58:59], 0, v[66:67]
	v_or_b32_e32 v42, 32, v39
	v_lshl_add_u64 v[116:117], v[66:67], 0, s[44:45]
	v_mad_i64_i32 v[66:67], s[48:49], v44, s46, 0
	v_or_b32_e32 v44, v42, v70
	v_or_b32_e32 v42, v42, v76
	v_lshrrev_b32_e32 v91, 1, v42
	v_and_b32_e32 v92, 4, v91
	v_bitop3_b32 v92, v92, s98, v70 bitop3:0x36
	v_lshlrev_b32_e32 v92, 5, v92
	v_lshlrev_b32_e32 v90, 8, v42
	v_xor_b32_e32 v92, 0x80, v92
	v_add3_u32 v90, 0, v92, v90
	v_or_b32_e32 v92, 64, v39
	v_or_b32_e32 v93, v92, v70
	v_or_b32_e32 v92, v92, v76
	v_lshrrev_b32_e32 v96, 1, v92
	v_and_b32_e32 v97, 4, v96
	v_mad_i64_i32 v[66:67], s[48:49], s42, v80, v[66:67]
	v_bitop3_b32 v97, v97, s98, v70 bitop3:0x36
	v_or3_b32 v66, v66, s50, v38
	v_or_b32_e32 v38, 0x51, v68
	v_lshlrev_b32_e32 v97, 5, v97
	v_lshl_add_u64 v[66:67], s[58:59], 0, v[66:67]
	v_cmp_gt_u32_e64 s[48:49], v38, v54
	v_lshlrev_b32_e32 v38, 5, v72
	v_lshlrev_b32_e32 v95, 8, v92
	v_xor_b32_e32 v97, 0x80, v97
	v_lshl_add_u64 v[118:119], v[66:67], 0, s[44:45]
	v_cmp_gt_u32_e64 s[44:45], v35, v54
	v_xad_u32 v149, v38, s22, v73
	s_movk_i32 s22, 0xa0
	v_add3_u32 v95, 0, v97, v95
	v_or_b32_e32 v97, 0x60, v39
	v_writelane_b32 v254, s44, 38
	v_xad_u32 v150, v38, s22, v73
	s_movk_i32 s22, 0xc0
	v_or_b32_e32 v76, v97, v76
	v_writelane_b32 v254, s45, 39
; #define GAS __attribute__((address_space(1)))
; __device__ __forceinline__ void p2_mlstm_chain(Frame& F, const Args& A, int ch) {
;     ...
;     f32x4 Cst[4]; f32x4 Nst = (f32x4){0.f, 0.f, 0.f, 0.f};
; #pragma unroll
;     for (int i = 0; i < 4; ++i) Cst[i] = (f32x4){0.f, 0.f, 0.f, 0.f};
;     ...
;         u32x2 og[8];
; #pragma unroll
;         for (int vb = 0; vb < 8; ++vb) og[vb] = *(const GAS u32x2*)(proj + (tg0 + t) * NP + 1024 + h * 128 + 16 * vb + 4 * fq);
	v_mad_i64_i32 v[34:35], s[44:45], v34, s46, 0
	v_mad_i64_i32 v[66:67], s[44:45], v36, s46, 0
	v_mad_u64_u32 v[46:47], s[44:45], v46, s46, 0
	v_xad_u32 v151, v38, s22, v73
	s_movk_i32 s22, 0x60
	v_lshrrev_b32_e32 v99, 1, v76
	v_cmp_gt_u32_e64 s[46:47], v37, v54
	v_or_b32_e32 v40, 0x50, v68
	v_mad_i64_i32 v[36:37], s[44:45], s42, v80, v[34:35]
	v_mad_i64_i32 v[34:35], s[44:45], s42, v80, v[66:67]
	v_mad_i64_i32 v[46:47], s[42:43], s42, v80, v[46:47]
	v_xad_u32 v152, v38, s22, v73
	s_movk_i32 s22, 0xe0
	v_and_b32_e32 v100, 4, v99
	v_xad_u32 v153, v38, s22, v73
	v_or3_b32 v46, v46, s50, v81
	v_cmp_gt_u32_e64 s[50:51], v40, v54
	v_or_b32_e32 v40, v39, v70
	v_add_u32_e32 v157, v73, v38
	v_xad_u32 v159, v38, 32, v73
	v_xad_u32 v160, v38, 64, v73
	v_or_b32_e32 v38, v68, v70
	v_or_b32_e32 v98, v97, v70
	v_bitop3_b32 v70, v100, s98, v70 bitop3:0x36
	v_lshlrev_b32_e32 v156, 8, v40
	v_lshlrev_b32_e32 v158, 8, v44
	v_lshl_add_u32 v163, v40, 7, v75
	v_and_or_b32 v40, v89, 1, v77
	v_lshl_add_u32 v170, v44, 7, v75
	v_and_or_b32 v44, v91, 1, v77
	v_lshl_add_u32 v94, v93, 8, v71
	v_lshl_add_u32 v173, v93, 7, v75
	v_and_or_b32 v93, v96, 1, v77
	v_lshlrev_b32_e32 v70, 5, v70
	v_and_or_b32 v77, v99, 1, v77
	s_add_i32 s7, 0, 0x14800
	v_lshl_add_u64 v[46:47], s[58:59], 0, v[46:47]
	s_mov_b64 s[42:43], 0x27000880
	v_lshlrev_b32_e32 v162, 5, v74
	v_lshlrev_b32_e32 v166, 5, v40
	v_lshlrev_b32_e32 v172, 5, v44
	v_lshlrev_b32_e32 v175, 5, v93
	v_lshlrev_b32_e32 v97, 8, v76
	v_xor_b32_e32 v70, 0x80, v70
	v_lshlrev_b32_e32 v178, 5, v77
	v_add_u32_e32 v45, 0, v63
	v_lshrrev_b32_e32 v233, 7, v0
	v_cmp_eq_u32_e64 s[98:99], 0, v233
	s_and_saveexec_b64 s[100:101], s[98:99]
	v_lshlrev_b32_e32 v232, 2, v0
	global_load_dword v233, v232, s[4:5]
	v_add_u32_e32 v232, 0x1c000, v232
	s_waitcnt vmcnt(0)
	ds_write_b32 v232, v233
	s_or_b64 exec, exec, s[100:101]
	s_sub_i32 s98, 11, s93
	s_cmp_lt_u32 s93, 4
	s_cselect_b32 s98, s93, s98
	v_bfe_u32 v252, v0, 4, 2
	v_lshlrev_b32_e32 v252, 4, v252
	v_add_u32_e32 v252, 0x1c000, v252
	v_lshl_add_u64 v[108:109], s[4:5], 0, v[106:107]
	v_cmp_eq_u32_e64 s[4:5], 0, v64
	v_lshl_add_u32 v148, v54, 2, s7
	v_cmp_gt_u32_e64 s[6:7], v68, v54
	v_cmp_lt_u32_e64 s[8:9], v68, v54
	v_lshl_add_u64 v[120:121], v[46:47], 0, s[42:43]
	v_or_b32_e32 v66, 0x53, v68
	v_or_b32_e32 v67, 0x52, v68
	v_or_b32_e32 v72, 0x61, v68
	v_or_b32_e32 v80, 0x60, v68
	v_or_b32_e32 v81, 0x63, v68
	v_or_b32_e32 v82, 0x62, v68
	v_or_b32_e32 v83, 0x71, v68
	v_or_b32_e32 v84, 0x70, v68
	v_or_b32_e32 v85, 0x73, v68
	v_or_b32_e32 v86, 0x72, v68
	v_lshlrev_b32_e32 v154, 2, v69
	v_lshlrev_b32_e32 v155, 2, v79
	v_lshl_add_u32 v161, v38, 8, v75
	v_xor_b32_e32 v38, 32, v162
	v_xor_b32_e32 v46, 64, v162
	v_xor_b32_e32 v47, 0x60, v162
	v_xor_b32_e32 v68, 0x80, v162
	v_xor_b32_e32 v69, 0xa0, v162
	v_xor_b32_e32 v73, 0xc0, v162
	v_xor_b32_e32 v74, 0xe0, v162
	v_add_u32_e32 v79, v71, v156
	v_lshl_add_u32 v164, v87, 7, v75
	v_lshlrev_b32_e32 v165, 5, v78
	v_xor_b32_e32 v40, 32, v166
	v_xor_b32_e32 v78, 64, v166
	v_xor_b32_e32 v87, 0x60, v166
	v_add_u32_e32 v89, v71, v158
	v_lshl_add_u32 v171, v42, 7, v75
	v_xor_b32_e32 v42, 32, v172
	v_xor_b32_e32 v44, 64, v172
	v_xor_b32_e32 v91, 0x60, v172
	v_lshl_add_u32 v174, v92, 7, v75
	v_xor_b32_e32 v92, 32, v175
	v_xor_b32_e32 v93, 64, v175
	v_xor_b32_e32 v96, 0x60, v175
	v_lshl_add_u32 v71, v98, 8, v71
	v_add3_u32 v70, 0, v70, v97
	v_lshl_add_u32 v176, v98, 7, v75
	v_lshl_add_u32 v177, v76, 7, v75
	v_xor_b32_e32 v75, 32, v178
	v_xor_b32_e32 v76, 64, v178
	v_xor_b32_e32 v77, 0x60, v178
	v_lshlrev_b32_e32 v64, 2, v64
	v_or3_b32 v36, v36, s60, v63
	v_or3_b32 v34, v34, s60, v63
	v_xor_b32_e32 v167, 32, v165
	v_xor_b32_e32 v168, 64, v165
	v_xor_b32_e32 v169, 0x60, v165
	v_add_u32_e32 v179, 0x15000, v65
	v_lshl_or_b32 v180, s98, 6, v64
	v_lshl_add_u64 v[122:123], s[58:59], 0, v[36:37]
	v_lshl_add_u64 v[124:125], s[58:59], 0, v[34:35]
	v_mov_b32_e32 v34, v107
	v_mov_b32_e32 v35, v107
	v_mov_b32_e32 v36, v107
	v_mov_b32_e32 v37, v107
	v_add_u32_e32 v181, v45, v48
	v_add_u32_e32 v182, v52, v41
	v_add_u32_e32 v183, v45, v53
	v_add_u32_e32 v184, v57, v41
	v_add_u32_e32 v185, v59, v41
	v_add_u32_e32 v186, v60, v41
	v_add_u32_e32 v187, v61, v41
	v_add_u32_e32 v188, v62, v41
	v_add_u32_e32 v189, v50, v51
	v_mov_b32_e32 v190, 0x358637bd
	v_add_u32_e32 v191, v79, v43
	v_add_u32_e32 v192, v88, v43
	v_add_u32_e32 v193, v164, v40
	v_add_u32_e32 v194, v164, v78
	v_add_u32_e32 v195, v164, v87
	v_add_u32_e32 v196, v89, v43
	v_add_u32_e32 v197, v90, v43
	v_add_u32_e32 v198, v171, v42
	v_add_u32_e32 v199, v171, v44
	v_add_u32_e32 v200, v171, v91
	v_add_u32_e32 v201, v94, v43
	v_add_u32_e32 v202, v95, v43
	v_add_u32_e32 v203, v174, v92
	v_add_u32_e32 v204, v174, v93
	v_add_u32_e32 v205, v174, v96
	v_add_u32_e32 v206, v71, v43
	v_add_u32_e32 v207, v70, v43
	v_add_u32_e32 v208, v177, v75
	v_add_u32_e32 v209, v177, v76
	v_add_u32_e32 v210, v177, v77
	v_add_u32_e32 v211, v49, v39
	v_add_u32_e32 v212, v55, v56
	v_add_u32_e32 v213, v55, v58
	v_add_u32_e32 v214, v161, v38
	v_add_u32_e32 v215, v161, v46
	v_add_u32_e32 v216, v161, v47
	v_add_u32_e32 v217, v161, v68
	v_add_u32_e32 v218, v161, v69
	v_add_u32_e32 v219, v161, v73
	v_add_u32_e32 v220, v161, v74
	v_mov_b32_e32 v50, v107
	v_mov_b32_e32 v51, v107
	v_mov_b32_e32 v52, v107
	v_mov_b32_e32 v53, v107
	v_mov_b32_e32 v46, v107
	v_mov_b32_e32 v47, v107
	v_mov_b32_e32 v48, v107
	v_mov_b32_e32 v49, v107
	v_mov_b32_e32 v42, v107
	v_mov_b32_e32 v43, v107
	v_mov_b32_e32 v44, v107
	v_mov_b32_e32 v45, v107
	v_mov_b32_e32 v38, v107
	v_mov_b32_e32 v39, v107
	v_mov_b32_e32 v40, v107
	v_mov_b32_e32 v41, v107
	v_cmp_gt_u32_e64 s[86:87], v66, v54
	v_cmp_gt_u32_e64 s[90:91], v67, v54
	v_cmp_gt_u32_e64 s[44:45], v72, v54
	v_cmp_gt_u32_e64 s[94:95], v80, v54
	v_cmp_gt_u32_e64 s[60:61], v81, v54
	v_cmp_gt_u32_e64 s[62:63], v82, v54
	v_cmp_gt_u32_e64 s[64:65], v83, v54
	v_cmp_gt_u32_e64 s[66:67], v84, v54
	v_cmp_gt_u32_e64 s[68:69], v85, v54
	v_cmp_gt_u32_e64 s[70:71], v86, v54
	s_mov_b64 s[42:43], 0
	s_mov_b32 s22, 0x3e000000
	global_load_dwordx2 v[140:141], v[120:121], off offset:-128
	global_load_dwordx2 v[138:139], v[120:121], off offset:-96
	global_load_dwordx2 v[136:137], v[120:121], off offset:-64
	global_load_dwordx2 v[134:135], v[120:121], off offset:-32
	global_load_dwordx2 v[132:133], v[120:121], off
	global_load_dwordx2 v[130:131], v[120:121], off offset:32
	global_load_dwordx2 v[128:129], v[120:121], off offset:64
	global_load_dwordx2 v[126:127], v[120:121], off offset:96
	s_branch .LBB0_378

; __device__ __forceinline__ void p2_mlstm_chain(Frame& F, const Args& A, int ch) {
;     ...
;     }
;     __syncthreads();
; }
.LBB0_437:
	v_readlane_b32 s72, v254, 8
	v_readlane_b32 s73, v254, 9
	s_waitcnt lgkmcnt(0)
	s_barrier
	v_readfirstlane_b32 s68, v0
	s_lshl_b32 s44, s93, 4
	s_cmpk_gt_u32 s68, 0x7f
	s_cselect_b64 s[14:15], -1, 0
	s_cmpk_lt_u32 s68, 0x100
	s_cselect_b64 s[40:41], -1, 0
	s_cmpk_gt_u32 s68, 0xff
	s_cselect_b64 s[18:19], -1, 0
	s_cmpk_gt_u32 s68, 0x17f
	s_cselect_b64 s[20:21], -1, 0
